# v045 + ln2 row mean/variance wave sums: 6 ds_bpermute round trips each -> v_add_f32_dpp butterfly + row_bcast + v_readlane
# speedup vs baseline: 1.0032x; 1.0002x over previous
; __device__ __forceinline__ float bflo(unsigned w) { return __uint_as_float(w << 16); }
; __device__ __forceinline__ float bfhi(unsigned w) { return __uint_as_float(w & 0xffff0000u); }
; template <bool HQ = false>
; __device__ __forceinline__ void ln2_phase(const bf16_t* h1b, const bf16_t* zs, float* out, const float* gam, const float* bet, int G, int b, const unsigned* xqs = nullptr, const float* sx = nullptr) {
;     ...
;     for (int row0 = gw; row0 < S_; row0 += R * NGW) {
;         f32x4 v[R][8]; float sum[R], sq[R];
; #pragma unroll
;         for (int q = 0; q < R; ++q) {
;             const int row = min(row0 + q * NGW, S_ - 1);
;             sum[q] = 0.f;
; #pragma unroll
;             for (int j = 0; j < 8; ++j) {
;                 const u32x2 zw = *(const u32x2*)(zs + (size_t)row * D_ + 256 * j + 4 * lane);
;                 if (HQ) { const int hq = (int)xqs[((size_t)j * S_ + row) * 64 + lane]; const float hs = DN_ALPHA * sx[row];
;                     v[q][j] = (f32x4){hs * (float)((hq << 24) >> 24) + bflo(zw.x), hs * (float)((hq << 16) >> 24) + bfhi(zw.x), hs * (float)((hq << 8) >> 24) + bflo(zw.y), hs * (float)(hq >> 24) + bfhi(zw.y)}; }
;                 else { const u32x2 hw = *(const u32x2*)(h1b + (size_t)row * D_ + 256 * j + 4 * lane);
;                     v[q][j] = (f32x4){DN_ALPHA * bflo(hw.x) + bflo(zw.x), DN_ALPHA * bfhi(hw.x) + bfhi(zw.x), DN_ALPHA * bflo(hw.y) + bflo(zw.y), DN_ALPHA * bfhi(hw.y) + bfhi(zw.y)}; }
;                 sum[q] += (v[q][j].x + v[q][j].y) + (v[q][j].z + v[q][j].w);
.LBB0_1004:
	v_lshl_add_u64 v[72:73], s[92:93], 0, v[70:71]
	v_add_co_u32_e64 v84, s[0:1], s3, v72
	v_lshl_add_u64 v[74:75], s[92:93], 0, v[68:69]
	s_nop 0
	v_addc_co_u32_e64 v85, s[0:1], 0, v73, s[0:1]
	v_add_co_u32_e64 v86, s[0:1], s16, v72
	v_add_co_u32_e32 v74, vcc, 0x18800000, v74
	s_nop 0
	v_addc_co_u32_e64 v87, s[0:1], 0, v73, s[0:1]
	v_add_co_u32_e64 v88, s[0:1], s17, v72
	v_addc_co_u32_e32 v75, vcc, 0, v75, vcc
	s_nop 0
	v_addc_co_u32_e64 v89, s[0:1], 0, v73, s[0:1]
	v_add_co_u32_e64 v90, s[0:1], s18, v72
	s_add_u32 s12, s92, s14
	s_nop 0
	v_addc_co_u32_e64 v91, s[0:1], 0, v73, s[0:1]
	v_add_co_u32_e64 v92, s[0:1], s19, v72
	s_addc_u32 s13, s93, s15
	s_nop 0
	v_addc_co_u32_e64 v93, s[0:1], 0, v73, s[0:1]
	v_add_co_u32_e64 v94, s[0:1], s20, v72
	global_load_dword v83, v65, s[12:13]
	s_nop 0
	v_addc_co_u32_e64 v95, s[0:1], 0, v73, s[0:1]
	v_add_co_u32_e64 v96, s[0:1], s21, v72
	v_add_co_u32_e32 v72, vcc, 0x6000000, v72
	s_nop 0
	v_addc_co_u32_e64 v97, s[0:1], 0, v73, s[0:1]
	v_addc_co_u32_e32 v73, vcc, 0, v73, vcc
	global_load_dwordx2 v[98:99], v[74:75], off
	global_load_dwordx2 v[100:101], v[74:75], off offset:512
	global_load_dwordx2 v[102:103], v[74:75], off offset:1024
	global_load_dwordx2 v[104:105], v[74:75], off offset:1536
	global_load_dwordx2 v[106:107], v[74:75], off offset:2048
	global_load_dwordx2 v[108:109], v[74:75], off offset:2560
	global_load_dwordx2 v[110:111], v[74:75], off offset:3072
	global_load_dwordx2 v[112:113], v[74:75], off offset:3584
	global_load_dword v116, v[72:73], off
	global_load_dword v120, v[84:85], off
	global_load_dword v124, v[86:87], off
	global_load_dword v128, v[88:89], off
	global_load_dword v132, v[90:91], off
	global_load_dword v136, v[92:93], off
	global_load_dword v140, v[94:95], off
	global_load_dword v144, v[96:97], off
	s_add_i32 s2, s2, s62
	s_add_u32 s14, s14, s4
	s_addc_u32 s15, s15, s5
	v_lshl_add_u64 v[68:69], v[68:69], 0, s[8:9]
	v_lshl_add_u64 v[70:71], v[70:71], 0, s[10:11]
	s_cmpk_lt_i32 s2, 0x4000
	s_waitcnt vmcnt(16)
	v_mul_f32_e32 v72, 0x3f9837f0, v83
	s_waitcnt vmcnt(15)
	v_lshlrev_b32_e32 v74, 16, v98
	s_waitcnt vmcnt(7)
	v_cvt_f32_i32_sdwa v115, sext(v116) dst_sel:DWORD dst_unused:UNUSED_PAD src0_sel:BYTE_1
	v_cvt_f32_i32_sdwa v114, sext(v116) dst_sel:DWORD dst_unused:UNUSED_PAD src0_sel:BYTE_0
	v_cvt_f32_i32_sdwa v117, sext(v116) dst_sel:DWORD dst_unused:UNUSED_PAD src0_sel:BYTE_3
	v_cvt_f32_i32_sdwa v116, sext(v116) dst_sel:DWORD dst_unused:UNUSED_PAD src0_sel:BYTE_2
	s_waitcnt vmcnt(6)
	v_cvt_f32_i32_sdwa v119, sext(v120) dst_sel:DWORD dst_unused:UNUSED_PAD src0_sel:BYTE_1
	v_cvt_f32_i32_sdwa v118, sext(v120) dst_sel:DWORD dst_unused:UNUSED_PAD src0_sel:BYTE_0
	v_cvt_f32_i32_sdwa v121, sext(v120) dst_sel:DWORD dst_unused:UNUSED_PAD src0_sel:BYTE_3
	v_cvt_f32_i32_sdwa v120, sext(v120) dst_sel:DWORD dst_unused:UNUSED_PAD src0_sel:BYTE_2
	s_waitcnt vmcnt(5)
	v_cvt_f32_i32_sdwa v123, sext(v124) dst_sel:DWORD dst_unused:UNUSED_PAD src0_sel:BYTE_1
	v_cvt_f32_i32_sdwa v122, sext(v124) dst_sel:DWORD dst_unused:UNUSED_PAD src0_sel:BYTE_0
	v_cvt_f32_i32_sdwa v125, sext(v124) dst_sel:DWORD dst_unused:UNUSED_PAD src0_sel:BYTE_3
	v_cvt_f32_i32_sdwa v124, sext(v124) dst_sel:DWORD dst_unused:UNUSED_PAD src0_sel:BYTE_2
	s_waitcnt vmcnt(4)
	v_cvt_f32_i32_sdwa v127, sext(v128) dst_sel:DWORD dst_unused:UNUSED_PAD src0_sel:BYTE_1
	v_cvt_f32_i32_sdwa v126, sext(v128) dst_sel:DWORD dst_unused:UNUSED_PAD src0_sel:BYTE_0
	v_cvt_f32_i32_sdwa v129, sext(v128) dst_sel:DWORD dst_unused:UNUSED_PAD src0_sel:BYTE_3
	v_cvt_f32_i32_sdwa v128, sext(v128) dst_sel:DWORD dst_unused:UNUSED_PAD src0_sel:BYTE_2
	s_waitcnt vmcnt(3)
	v_cvt_f32_i32_sdwa v131, sext(v132) dst_sel:DWORD dst_unused:UNUSED_PAD src0_sel:BYTE_1
	v_cvt_f32_i32_sdwa v130, sext(v132) dst_sel:DWORD dst_unused:UNUSED_PAD src0_sel:BYTE_0
	v_cvt_f32_i32_sdwa v133, sext(v132) dst_sel:DWORD dst_unused:UNUSED_PAD src0_sel:BYTE_3
	v_cvt_f32_i32_sdwa v132, sext(v132) dst_sel:DWORD dst_unused:UNUSED_PAD src0_sel:BYTE_2
	s_waitcnt vmcnt(2)
	v_cvt_f32_i32_sdwa v135, sext(v136) dst_sel:DWORD dst_unused:UNUSED_PAD src0_sel:BYTE_1
	v_cvt_f32_i32_sdwa v134, sext(v136) dst_sel:DWORD dst_unused:UNUSED_PAD src0_sel:BYTE_0
	v_cvt_f32_i32_sdwa v137, sext(v136) dst_sel:DWORD dst_unused:UNUSED_PAD src0_sel:BYTE_3
	v_cvt_f32_i32_sdwa v136, sext(v136) dst_sel:DWORD dst_unused:UNUSED_PAD src0_sel:BYTE_2
	s_waitcnt vmcnt(1)
	v_cvt_f32_i32_sdwa v139, sext(v140) dst_sel:DWORD dst_unused:UNUSED_PAD src0_sel:BYTE_1
	v_cvt_f32_i32_sdwa v138, sext(v140) dst_sel:DWORD dst_unused:UNUSED_PAD src0_sel:BYTE_0
	v_cvt_f32_i32_sdwa v141, sext(v140) dst_sel:DWORD dst_unused:UNUSED_PAD src0_sel:BYTE_3
	v_cvt_f32_i32_sdwa v140, sext(v140) dst_sel:DWORD dst_unused:UNUSED_PAD src0_sel:BYTE_2
	s_waitcnt vmcnt(0)
; __device__ __forceinline__ float bflo(unsigned w) { return __uint_as_float(w << 16); }
; __device__ __forceinline__ float bfhi(unsigned w) { return __uint_as_float(w & 0xffff0000u); }
; __device__ __forceinline__ float wave_sum(float v) {
; #pragma unroll
;     for (int o = 1; o < 64; o <<= 1) v += __shfl_xor(v, o);
;     return v;
; template <bool HQ = false>
; __device__ __forceinline__ void ln2_phase(const bf16_t* h1b, const bf16_t* zs, float* out, const float* gam, const float* bet, int G, int b, const unsigned* xqs = nullptr, const float* sx = nullptr) {
;     ...
;                 const u32x2 zw = *(const u32x2*)(zs + (size_t)row * D_ + 256 * j + 4 * lane);
;                 if (HQ) { const int hq = (int)xqs[((size_t)j * S_ + row) * 64 + lane]; const float hs = DN_ALPHA * sx[row];
;                     v[q][j] = (f32x4){hs * (float)((hq << 24) >> 24) + bflo(zw.x), hs * (float)((hq << 16) >> 24) + bfhi(zw.x), hs * (float)((hq << 8) >> 24) + bflo(zw.y), hs * (float)(hq >> 24) + bfhi(zw.y)}; }
;                 else { const u32x2 hw = *(const u32x2*)(h1b + (size_t)row * D_ + 256 * j + 4 * lane);
;                     v[q][j] = (f32x4){DN_ALPHA * bflo(hw.x) + bflo(zw.x), DN_ALPHA * bfhi(hw.x) + bfhi(zw.x), DN_ALPHA * bflo(hw.y) + bflo(zw.y), DN_ALPHA * bfhi(hw.y) + bfhi(zw.y)}; }
;                 sum[q] += (v[q][j].x + v[q][j].y) + (v[q][j].z + v[q][j].w);
;             }
;         }
; #pragma unroll
;         for (int q = 0; q < R; ++q) sum[q] = wave_sum(sum[q]) * (1.0f / D_);
	v_cvt_f32_i32_sdwa v143, sext(v144) dst_sel:DWORD dst_unused:UNUSED_PAD src0_sel:BYTE_1
	v_cvt_f32_i32_sdwa v142, sext(v144) dst_sel:DWORD dst_unused:UNUSED_PAD src0_sel:BYTE_0
	v_cvt_f32_i32_sdwa v145, sext(v144) dst_sel:DWORD dst_unused:UNUSED_PAD src0_sel:BYTE_3
	v_cvt_f32_i32_sdwa v144, sext(v144) dst_sel:DWORD dst_unused:UNUSED_PAD src0_sel:BYTE_2
	v_and_b32_e32 v75, 0xffff0000, v98
	v_lshlrev_b32_e32 v84, 16, v99
	v_and_b32_e32 v85, 0xffff0000, v99
	v_lshlrev_b32_e32 v86, 16, v100
	v_and_b32_e32 v87, 0xffff0000, v100
	v_lshlrev_b32_e32 v88, 16, v101
	v_and_b32_e32 v89, 0xffff0000, v101
	v_lshlrev_b32_e32 v90, 16, v102
	v_and_b32_e32 v91, 0xffff0000, v102
	v_lshlrev_b32_e32 v92, 16, v103
	v_and_b32_e32 v93, 0xffff0000, v103
	v_lshlrev_b32_e32 v94, 16, v104
	v_and_b32_e32 v95, 0xffff0000, v104
	v_lshlrev_b32_e32 v96, 16, v105
	v_and_b32_e32 v97, 0xffff0000, v105
	v_lshlrev_b32_e32 v98, 16, v106
	v_and_b32_e32 v99, 0xffff0000, v106
	v_lshlrev_b32_e32 v100, 16, v107
	v_and_b32_e32 v101, 0xffff0000, v107
	v_lshlrev_b32_e32 v102, 16, v108
	v_and_b32_e32 v103, 0xffff0000, v108
	v_lshlrev_b32_e32 v104, 16, v109
	v_and_b32_e32 v105, 0xffff0000, v109
	v_lshlrev_b32_e32 v106, 16, v110
	v_and_b32_e32 v107, 0xffff0000, v110
	v_lshlrev_b32_e32 v108, 16, v111
	v_and_b32_e32 v109, 0xffff0000, v111
	v_lshlrev_b32_e32 v110, 16, v112
	v_and_b32_e32 v111, 0xffff0000, v112
	v_lshlrev_b32_e32 v112, 16, v113
	v_and_b32_e32 v113, 0xffff0000, v113
	v_pk_fma_f32 v[74:75], v[72:73], v[114:115], v[74:75] op_sel_hi:[0,1,1]
	v_pk_fma_f32 v[84:85], v[72:73], v[116:117], v[84:85] op_sel_hi:[0,1,1]
	v_pk_fma_f32 v[86:87], v[72:73], v[118:119], v[86:87] op_sel_hi:[0,1,1]
	v_pk_fma_f32 v[88:89], v[72:73], v[120:121], v[88:89] op_sel_hi:[0,1,1]
	v_pk_fma_f32 v[90:91], v[72:73], v[122:123], v[90:91] op_sel_hi:[0,1,1]
	v_pk_fma_f32 v[92:93], v[72:73], v[124:125], v[92:93] op_sel_hi:[0,1,1]
	v_pk_fma_f32 v[94:95], v[72:73], v[126:127], v[94:95] op_sel_hi:[0,1,1]
	v_pk_fma_f32 v[96:97], v[72:73], v[128:129], v[96:97] op_sel_hi:[0,1,1]
	v_pk_fma_f32 v[98:99], v[72:73], v[130:131], v[98:99] op_sel_hi:[0,1,1]
	v_pk_fma_f32 v[100:101], v[72:73], v[132:133], v[100:101] op_sel_hi:[0,1,1]
	v_pk_fma_f32 v[102:103], v[72:73], v[134:135], v[102:103] op_sel_hi:[0,1,1]
	v_pk_fma_f32 v[104:105], v[72:73], v[136:137], v[104:105] op_sel_hi:[0,1,1]
	v_pk_fma_f32 v[106:107], v[72:73], v[138:139], v[106:107] op_sel_hi:[0,1,1]
	v_pk_fma_f32 v[108:109], v[72:73], v[140:141], v[108:109] op_sel_hi:[0,1,1]
	v_pk_fma_f32 v[110:111], v[72:73], v[142:143], v[110:111] op_sel_hi:[0,1,1]
	v_pk_fma_f32 v[72:73], v[72:73], v[144:145], v[112:113] op_sel_hi:[0,1,1]
	v_mov_b32_e32 v112, v74
	v_mov_b32_e32 v113, v86
	v_mov_b32_e32 v114, v75
	v_mov_b32_e32 v115, v87
	v_mov_b32_e32 v116, v85
	v_mov_b32_e32 v117, v89
	v_mov_b32_e32 v118, v84
	v_mov_b32_e32 v119, v88
	v_mov_b32_e32 v120, v90
	v_mov_b32_e32 v121, v93
	v_pk_mov_b32 v[122:123], v[90:91], v[92:93] op_sel:[1,0]
	v_pk_add_f32 v[112:113], v[112:113], v[114:115]
	v_pk_add_f32 v[114:115], v[116:117], v[118:119]
	v_pk_add_f32 v[116:117], v[120:121], v[122:123]
	v_pk_add_f32 v[112:113], v[112:113], v[114:115]
	v_pk_add_f32 v[124:125], v[94:95], v[94:95] op_sel:[0,1] op_sel_hi:[1,0]
	v_pk_add_f32 v[126:127], v[96:97], v[96:97] op_sel:[1,0] op_sel_hi:[0,1]
	v_pk_add_f32 v[114:115], v[116:117], v[116:117] op_sel:[0,1] op_sel_hi:[1,0]
	v_add_f32_e32 v83, 0, v112
	v_mov_b32_e32 v129, v98
	v_mov_b32_e32 v125, v101
	v_mov_b32_e32 v127, v100
	v_mov_b32_e32 v115, v99
	v_add_f32_e32 v128, v83, v113
	v_mov_b32_e32 v130, v102
	v_mov_b32_e32 v131, v105
	v_pk_mov_b32 v[132:133], v[102:103], v[104:105] op_sel:[1,0]
	v_pk_add_f32 v[116:117], v[124:125], v[126:127]
	v_pk_add_f32 v[112:113], v[128:129], v[114:115]
	v_pk_add_f32 v[118:119], v[130:131], v[132:133]
	v_pk_add_f32 v[112:113], v[112:113], v[116:117]
	v_pk_add_f32 v[134:135], v[106:107], v[106:107] op_sel:[0,1] op_sel_hi:[1,0]
	v_pk_add_f32 v[136:137], v[108:109], v[108:109] op_sel:[1,0] op_sel_hi:[0,1]
	v_pk_add_f32 v[118:119], v[118:119], v[118:119] op_sel:[0,1] op_sel_hi:[1,0]
	v_pk_add_f32 v[112:113], v[112:113], v[112:113] op_sel:[0,1] op_sel_hi:[1,0]
	v_mov_b32_e32 v135, v73
	v_mov_b32_e32 v137, v72
	v_mov_b32_e32 v119, v111
	v_mov_b32_e32 v113, v110
	v_pk_add_f32 v[120:121], v[134:135], v[136:137]
	v_pk_add_f32 v[112:113], v[112:113], v[118:119]
	s_nop 0
	v_pk_add_f32 v[112:113], v[112:113], v[120:121]
	s_nop 0
	v_add_f32_e32 v83, v112, v113
	s_nop 1
	v_add_f32_dpp v83, v83, v83 quad_perm:[1,0,3,2] row_mask:0xf bank_mask:0xf
	s_nop 1
	v_add_f32_dpp v83, v83, v83 quad_perm:[2,3,0,1] row_mask:0xf bank_mask:0xf
	s_nop 1
	v_add_f32_dpp v83, v83, v83 row_half_mirror row_mask:0xf bank_mask:0xf
	s_nop 1
	v_add_f32_dpp v83, v83, v83 row_mirror row_mask:0xf bank_mask:0xf
	s_nop 1
	v_add_f32_dpp v83, v83, v83 row_bcast:15 row_mask:0xa bank_mask:0xf
	s_nop 1
	v_add_f32_dpp v83, v83, v83 row_bcast:31 row_mask:0xc bank_mask:0xf
	s_waitcnt lgkmcnt(0)
; template <bool HQ = false>
; __device__ __forceinline__ void ln2_phase(const bf16_t* h1b, const bf16_t* zs, float* out, const float* gam, const float* bet, int G, int b, const unsigned* xqs = nullptr, const float* sx = nullptr) {
;     ...
;         for (int q = 0; q < R; ++q) sum[q] = wave_sum(sum[q]) * (1.0f / D_);
; #pragma unroll
;         for (int q = 0; q < R; ++q) { sq[q] = 0.f;
; #pragma unroll
;             for (int j = 0; j < 8; ++j) { v[q][j] = v[q][j] - sum[q]; sq[q] += (v[q][j].x * v[q][j].x + v[q][j].y * v[q][j].y) + (v[q][j].z * v[q][j].z + v[q][j].w * v[q][j].w); } }
; #pragma unroll
;         for (int q = 0; q < R; ++q) sq[q] = 1.0f / sqrtf(wave_sum(sq[q]) * (1.0f / D_) + LN_EPS);
	s_nop 1
	v_readlane_b32 s98, v83, 63
	s_nop 1
	v_mov_b32_e32 v83, s98
	v_fmamk_f32 v85, v83, 0xba000000, v85
	v_fmamk_f32 v75, v83, 0xba000000, v75
	v_fmamk_f32 v89, v83, 0xba000000, v89
	v_fmamk_f32 v87, v83, 0xba000000, v87
	v_fmac_f32_e32 v84, 0xba000000, v83
	v_fmac_f32_e32 v74, 0xba000000, v83
	v_fmac_f32_e32 v88, 0xba000000, v83
	v_fmac_f32_e32 v86, 0xba000000, v83
	v_fmamk_f32 v91, v83, 0xba000000, v91
	v_fmac_f32_e32 v90, 0xba000000, v83
	v_fmamk_f32 v93, v83, 0xba000000, v93
	v_fmac_f32_e32 v92, 0xba000000, v83
	v_mov_b32_e32 v114, v75
	v_mov_b32_e32 v115, v87
	v_mov_b32_e32 v118, v85
	v_mov_b32_e32 v119, v89
	v_mov_b32_e32 v112, v74
	v_mov_b32_e32 v113, v86
	v_mov_b32_e32 v116, v84
	v_mov_b32_e32 v117, v88
	v_pk_mul_f32 v[120:121], v[92:93], v[92:93]
	v_pk_mul_f32 v[122:123], v[90:91], v[90:91]
	v_pk_mul_f32 v[114:115], v[114:115], v[114:115]
	v_pk_mul_f32 v[118:119], v[118:119], v[118:119]
	v_fmac_f32_e32 v94, 0xba000000, v83
	v_fmac_f32_e32 v96, 0xba000000, v83
	v_pk_mov_b32 v[136:137], v[122:123], v[120:121] op_sel:[1,0]
	v_mov_b32_e32 v123, v121
	v_pk_fma_f32 v[112:113], v[112:113], v[112:113], v[114:115]
	v_pk_fma_f32 v[114:115], v[116:117], v[116:117], v[118:119]
	v_fmamk_f32 v95, v83, 0xba000000, v95
	v_fmamk_f32 v97, v83, 0xba000000, v97
	v_mul_f32_e32 v124, v94, v94
	v_mul_f32_e32 v126, v96, v96
	v_pk_add_f32 v[116:117], v[136:137], v[122:123]
	v_pk_add_f32 v[112:113], v[112:113], v[114:115]
	v_fmamk_f32 v101, v83, 0xba000000, v101
	v_fmac_f32_e32 v100, 0xba000000, v83
	v_fmamk_f32 v99, v83, 0xba000000, v99
	v_fmac_f32_e32 v98, 0xba000000, v83
	v_fmamk_f32 v103, v83, 0xba000000, v103
	v_fmac_f32_e32 v102, 0xba000000, v83
	v_fmamk_f32 v105, v83, 0xba000000, v105
	v_fmac_f32_e32 v104, 0xba000000, v83
	v_pk_fma_f32 v[120:121], v[94:95], v[94:95], v[124:125] op_sel_hi:[1,1,0]
	v_pk_fma_f32 v[124:125], v[96:97], v[96:97], v[126:127] op_sel_hi:[1,1,0]
	v_pk_add_f32 v[114:115], v[116:117], v[116:117] op_sel_hi:[0,1]
	v_pk_add_f32 v[112:113], v[112:113], v[112:113] op_sel_hi:[0,1]
	v_pk_mul_f32 v[128:129], v[104:105], v[104:105]
	v_pk_mul_f32 v[130:131], v[102:103], v[102:103]
	v_mul_f32_e32 v120, v98, v98
	v_mul_f32_e32 v124, v99, v99
	v_mul_f32_e32 v114, v100, v100
	v_mul_f32_e32 v112, v101, v101
	v_fmac_f32_e32 v106, 0xba000000, v83
	v_fmac_f32_e32 v108, 0xba000000, v83
	v_pk_mov_b32 v[126:127], v[130:131], v[128:129] op_sel:[1,0]
	v_mov_b32_e32 v131, v129
	v_pk_add_f32 v[116:117], v[120:121], v[124:125]
	v_pk_add_f32 v[112:113], v[114:115], v[112:113]
	v_fmamk_f32 v107, v83, 0xba000000, v107
	v_fmamk_f32 v109, v83, 0xba000000, v109
	v_mul_f32_e32 v132, v106, v106
	v_mul_f32_e32 v134, v108, v108
	v_pk_add_f32 v[118:119], v[126:127], v[130:131]
	v_pk_add_f32 v[112:113], v[116:117], v[112:113]
	v_fmamk_f32 v73, v83, 0xba000000, v73
	v_fmac_f32_e32 v72, 0xba000000, v83
	v_fmamk_f32 v111, v83, 0xba000000, v111
	v_fmac_f32_e32 v110, 0xba000000, v83
	v_pk_fma_f32 v[128:129], v[106:107], v[106:107], v[132:133] op_sel_hi:[1,1,0]
	v_pk_fma_f32 v[132:133], v[108:109], v[108:109], v[134:135] op_sel_hi:[1,1,0]
	v_pk_add_f32 v[118:119], v[118:119], v[118:119] op_sel_hi:[0,1]
	v_pk_add_f32 v[112:113], v[112:113], v[112:113] op_sel_hi:[0,1]
	v_mul_f32_e32 v128, v110, v110
	v_mul_f32_e32 v132, v111, v111
	v_mul_f32_e32 v118, v72, v72
	v_mul_f32_e32 v112, v73, v73
	v_pk_add_f32 v[120:121], v[128:129], v[132:133]
	v_pk_add_f32 v[112:113], v[118:119], v[112:113]
	s_nop 0
	v_pk_add_f32 v[112:113], v[120:121], v[112:113]
	s_nop 0
	v_add_f32_e32 v83, v112, v113
	s_nop 1
	v_add_f32_dpp v83, v83, v83 quad_perm:[1,0,3,2] row_mask:0xf bank_mask:0xf
	s_nop 1
	v_add_f32_dpp v83, v83, v83 quad_perm:[2,3,0,1] row_mask:0xf bank_mask:0xf
	s_nop 1
	v_add_f32_dpp v83, v83, v83 row_half_mirror row_mask:0xf bank_mask:0xf
	s_nop 1
	v_add_f32_dpp v83, v83, v83 row_mirror row_mask:0xf bank_mask:0xf
	s_nop 1
	v_add_f32_dpp v83, v83, v83 row_bcast:15 row_mask:0xa bank_mask:0xf
	s_nop 1
	v_add_f32_dpp v83, v83, v83 row_bcast:31 row_mask:0xc bank_mask:0xf
	s_waitcnt lgkmcnt(0)
; template <bool HQ = false>
; __device__ __forceinline__ void ln2_phase(const bf16_t* h1b, const bf16_t* zs, float* out, const float* gam, const float* bet, int G, int b, const unsigned* xqs = nullptr, const float* sx = nullptr) {
;     ...
;         for (int q = 0; q < R; ++q) sq[q] = 1.0f / sqrtf(wave_sum(sq[q]) * (1.0f / D_) + LN_EPS);
; #pragma unroll
;         for (int j = 0; j < 8; ++j) {
;             const f32x4 gg = gg8[j], bb = bb8[j];
; #pragma unroll
;             for (int q = 0; q < R; ++q) { const int row = row0 + q * NGW; if (row < S_) *(f32x4*)(out + (size_t)row * D_ + 256 * j + 4 * lane) = v[q][j] * sq[q] * gg + bb; }
;         }
	s_nop 1
	v_readlane_b32 s98, v83, 63
	s_nop 1
	v_mov_b32_e32 v83, s98
	v_fmamk_f32 v83, v83, 0x3a000000, v64
	v_mul_f32_e32 v112, 0x4f800000, v83
	v_cmp_gt_f32_e32 vcc, s22, v83
	s_nop 1
	v_cndmask_b32_e32 v83, v83, v112, vcc
	v_sqrt_f32_e32 v112, v83
	s_nop 0
	v_add_u32_e32 v113, -1, v112
	v_add_u32_e32 v114, 1, v112
	v_fma_f32 v115, -v113, v112, v83
	v_fma_f32 v116, -v114, v112, v83
	v_cmp_ge_f32_e64 s[0:1], 0, v115
	s_nop 1
	v_cndmask_b32_e64 v112, v112, v113, s[0:1]
	v_cmp_lt_f32_e64 s[0:1], 0, v116
	s_nop 1
	v_cndmask_b32_e64 v112, v112, v114, s[0:1]
	v_mul_f32_e32 v113, 0x37800000, v112
	v_cndmask_b32_e32 v112, v112, v113, vcc
	v_cmp_class_f32_e32 vcc, v83, v82
	s_nop 1
	v_cndmask_b32_e32 v83, v112, v83, vcc
	v_div_scale_f32 v112, s[0:1], v83, v83, 1.0
	v_rcp_f32_e32 v114, v112
	v_div_scale_f32 v113, vcc, 1.0, v83, 1.0
	v_fma_f32 v115, -v112, v114, 1.0
	v_fmac_f32_e32 v114, v115, v114
	v_mul_f32_e32 v115, v113, v114
	v_fma_f32 v116, -v112, v115, v113
	v_fmac_f32_e32 v115, v116, v114
	v_fma_f32 v112, -v112, v115, v113
	v_div_fmas_f32 v112, v112, v114, v115
	v_div_fixup_f32 v112, v112, v83, 1.0
	v_pk_mul_f32 v[114:115], v[74:75], v[112:113] op_sel_hi:[1,0]
	v_pk_mul_f32 v[74:75], v[84:85], v[112:113] op_sel_hi:[1,0]
	v_pk_mul_f32 v[84:85], v[86:87], v[112:113] op_sel_hi:[1,0]
	v_pk_mul_f32 v[86:87], v[88:89], v[112:113] op_sel_hi:[1,0]
	v_pk_mul_f32 v[88:89], v[90:91], v[112:113] op_sel_hi:[1,0]
	v_pk_mul_f32 v[90:91], v[92:93], v[112:113] op_sel_hi:[1,0]
	v_pk_mul_f32 v[92:93], v[94:95], v[112:113] op_sel_hi:[1,0]
	v_pk_mul_f32 v[94:95], v[96:97], v[112:113] op_sel_hi:[1,0]
	v_pk_mul_f32 v[96:97], v[98:99], v[112:113] op_sel_hi:[1,0]
	v_pk_mul_f32 v[98:99], v[100:101], v[112:113] op_sel_hi:[1,0]
	v_pk_mul_f32 v[100:101], v[102:103], v[112:113] op_sel_hi:[1,0]
	v_pk_mul_f32 v[102:103], v[104:105], v[112:113] op_sel_hi:[1,0]
	v_pk_mul_f32 v[104:105], v[106:107], v[112:113] op_sel_hi:[1,0]
	v_pk_mul_f32 v[106:107], v[108:109], v[112:113] op_sel_hi:[1,0]
	v_pk_mul_f32 v[108:109], v[110:111], v[112:113] op_sel_hi:[1,0]
	v_pk_mul_f32 v[110:111], v[72:73], v[112:113] op_sel_hi:[1,0]
	v_pk_fma_f32 v[74:75], v[2:3], v[74:75], v[6:7]
	v_pk_fma_f32 v[72:73], v[0:1], v[114:115], v[4:5]
	v_pk_fma_f32 v[86:87], v[10:11], v[86:87], v[14:15]
	v_pk_fma_f32 v[84:85], v[8:9], v[84:85], v[12:13]
	v_pk_fma_f32 v[90:91], v[18:19], v[90:91], v[22:23]
	v_pk_fma_f32 v[88:89], v[16:17], v[88:89], v[20:21]
	v_pk_fma_f32 v[94:95], v[26:27], v[94:95], v[30:31]
	v_pk_fma_f32 v[92:93], v[24:25], v[92:93], v[28:29]
	v_pk_fma_f32 v[98:99], v[34:35], v[98:99], v[42:43]
	v_pk_fma_f32 v[96:97], v[32:33], v[96:97], v[40:41]
	v_pk_fma_f32 v[102:103], v[38:39], v[102:103], v[46:47]
	v_pk_fma_f32 v[100:101], v[36:37], v[100:101], v[44:45]
	v_pk_fma_f32 v[106:107], v[50:51], v[106:107], v[58:59]
	v_pk_fma_f32 v[104:105], v[48:49], v[104:105], v[56:57]
	v_pk_fma_f32 v[110:111], v[54:55], v[110:111], v[62:63]
	v_pk_fma_f32 v[108:109], v[52:53], v[108:109], v[60:61]
	global_store_dwordx4 v[66:67], v[72:75], off offset:-4096
	global_store_dwordx4 v[66:67], v[84:87], off offset:-3072
	global_store_dwordx4 v[66:67], v[88:91], off offset:-2048
	global_store_dwordx4 v[66:67], v[92:95], off offset:-1024
	global_store_dwordx4 v[66:67], v[96:99], off
	global_store_dwordx4 v[66:67], v[100:103], off offset:1024
	global_store_dwordx4 v[66:67], v[104:107], off offset:2048
	global_store_dwordx4 v[66:67], v[108:111], off offset:3072
	v_lshl_add_u64 v[66:67], v[66:67], 0, s[6:7]
	s_cbranch_scc1 .LBB0_1004
